# baseline (speedup 1.0000x reference)
.LBB1_8:
	s_or_b64 exec, exec, s[12:13]
	s_mov_b32 s14, 0
	v_cmp_eq_u32_e32 vcc, 0, v0
	s_and_saveexec_b64 s[0:1], vcc
	v_mov_b32_e32 v1, 0
	ds_write_b32 v1, v1 offset:24832
	s_or_b64 exec, exec, s[0:1]
	s_lshr_b32 s0, s2, 1
	s_and_b32 s0, s0, 0x7fffffc
	s_and_b32 s1, s2, 3
	s_or_b32 s0, s0, s1
	s_bfe_u32 s16, s2, 0x10002
	s_lshl_b32 s2, s0, 5
	s_ashr_i32 s3, s2, 31
	s_lshl_b64 s[0:1], s[2:3], 7
	s_waitcnt lgkmcnt(0)
	s_add_u32 s0, s8, s0
	s_addc_u32 s1, s9, s1
	s_add_u32 s4, s0, 0x49000
	s_addc_u32 s5, s1, 0
	v_add_u32_e32 v5, 1, v2
	s_cmp_eq_u32 s16, 0
	v_lshlrev_b32_e32 v1, 9, v5
	s_cselect_b64 vcc, -1, 0
	v_add_u32_e32 v2, 0x4080, v6
	v_sub_u32_e32 v4, 0, v0
	v_and_b32_e32 v3, 0x3800, v1
	s_mov_b64 s[6:7], 0
	v_mov_b32_e32 v1, 0
	s_movk_i32 s15, 0xff7e
	s_movk_i32 s17, 0x80
	s_mov_b32 s18, 0
	s_barrier
	v_lshrrev_b32_e32 v4, 4, v0
	v_and_b32_e32 v5, 15, v0
	v_mul_u32_u24_e32 v4, 0x104, v4
	v_lshlrev_b32_e32 v5, 4, v5
	v_mov_b32_e32 v6, 0x4000400
	ds_write_b32 v4, v6 offset:16768
	v_mov_b32_e32 v106, v157
	v_mov_b32_e32 v107, v157
	v_mov_b32_e32 v100, 0xc47a0000
	v_mov_b32_e32 v104, v157
	v_mov_b32_e32 v105, v157
	v_mov_b64_e32 v[142:143], v[106:107]
	v_mov_b32_e32 v172, v157
	v_mov_b32_e32 v173, v157
	v_mov_b32_e32 v174, v157
	v_mov_b32_e32 v175, v157
	v_mov_b32_e32 v144, v157
	v_mov_b32_e32 v145, v157
	v_mov_b32_e32 v146, v157
	v_mov_b32_e32 v147, v157
	v_mov_b32_e32 v132, v157
	v_mov_b32_e32 v133, v157
	v_mov_b32_e32 v134, v157
	v_mov_b32_e32 v135, v157
	v_mov_b32_e32 v128, v157
	v_mov_b32_e32 v129, v157
	v_mov_b32_e32 v130, v157
	v_mov_b32_e32 v131, v157
	v_mov_b32_e32 v136, v157
	v_mov_b32_e32 v137, v157
	v_mov_b32_e32 v138, v157
	v_mov_b32_e32 v139, v157
	v_mov_b32_e32 v124, v157
	v_mov_b32_e32 v125, v157
	v_mov_b32_e32 v126, v157
	v_mov_b32_e32 v127, v157
	v_mov_b32_e32 v170, v157
	v_mov_b32_e32 v171, v157
	v_mov_b32_e32 v168, v157
	v_mov_b32_e32 v169, v157
	v_mov_b64_e32 v[140:141], v[104:105]
	v_mov_b32_e32 v144, 0
	v_mov_b32_e32 v145, 0
	v_mov_b32_e32 v146, 0
	v_mov_b32_e32 v147, 0
	v_mov_b32_e32 v148, 0xc47a0000
	v_mov_b32_e32 v149, 0xc47a0000
	v_mov_b32_e32 v150, 0xc47a0000
	v_mov_b32_e32 v151, 0xc47a0000
	v_mov_b32_e32 v152, 0
	v_mov_b32_e32 v153, 0
	v_mov_b32_e32 v154, 0
	v_mov_b32_e32 v155, 0
	s_waitcnt vmcnt(22)
	s_mov_b32 s0, 0xe0e0e0e0
	s_mov_b32 s1, 0x20202020
	s_mov_b32 s6, 0x01010101
	s_mov_b32 s7, 0x80808080
	v_and_b32_e32 v7, s0, v250
	v_xor_b32_e32 v7, s1, v7
	v_subrev_u32_e32 v9, s6, v7
	v_not_b32_e32 v7, v7
	v_and_b32_e32 v7, v9, v7
	v_and_b32_e32 v7, s7, v7
	v_and_b32_e32 v8, s0, v251
	v_xor_b32_e32 v8, s1, v8
	v_subrev_u32_e32 v9, s6, v8
	v_not_b32_e32 v8, v8
	v_and_b32_e32 v8, v9, v8
	v_and_b32_e32 v8, s7, v8
	v_or_b32_e32 v7, v7, v8
	v_bfe_u32 v8, v250, 0, 8
	v_bfe_u32 v9, v250, 8, 8
	v_min_u32_e32 v8, 64, v8
	v_min_u32_e32 v9, 64, v9
	v_lshlrev_b32_e32 v8, 4, v8
	v_lshlrev_b32_e32 v9, 20, v9
	v_or_b32_e32 v10, v8, v9
	v_bfe_u32 v8, v250, 16, 8
	v_bfe_u32 v9, v250, 24, 8
	v_min_u32_e32 v8, 64, v8
	v_min_u32_e32 v9, 64, v9
	v_lshlrev_b32_e32 v8, 4, v8
	v_lshlrev_b32_e32 v9, 20, v9
	v_or_b32_e32 v11, v8, v9
	v_bfe_u32 v8, v251, 0, 8
	v_bfe_u32 v9, v251, 8, 8
	v_min_u32_e32 v8, 64, v8
	v_min_u32_e32 v9, 64, v9
	v_lshlrev_b32_e32 v8, 4, v8
	v_lshlrev_b32_e32 v9, 20, v9
	v_or_b32_e32 v218, v8, v9
	v_bfe_u32 v8, v251, 16, 8
	v_bfe_u32 v9, v251, 24, 8
	v_min_u32_e32 v8, 64, v8
	v_min_u32_e32 v9, 64, v9
	v_lshlrev_b32_e32 v8, 4, v8
	v_lshlrev_b32_e32 v9, 20, v9
	v_or_b32_e32 v219, v8, v9
	s_cmp_eq_u32 s16, 0
	s_cbranch_scc0 .Ltok_bwd
	v_add_u32_e32 v4, v4, v5
	ds_write_b32 v4, v10 offset:16512
	ds_write_b32 v4, v11 offset:16516
	ds_write_b32 v4, v218 offset:16520
	ds_write_b32 v4, v219 offset:16524
	s_branch .Ltok_done

.Ltok_done:
	v_cmp_ne_u32_e32 vcc, 0, v7
	s_and_saveexec_b64 s[6:7], vcc
	v_mov_b32_e32 v1, 1
	v_mov_b32_e32 v2, 0
	ds_write_b32 v2, v1 offset:24832
	s_or_b64 exec, exec, s[6:7]
	s_mov_b32 s5, 0
	s_cmp_eq_u32 s16, 0
	s_cselect_b64 vcc, -1, 0
	v_mov_b32_e32 v157, 0
	s_waitcnt lgkmcnt(0)
	s_barrier
	s_and_b64 s[0:1], vcc, exec
	s_cselect_b32 s14, 0, 0x7f
	s_lshl_b32 s7, s16, 22
	s_add_u32 s0, s8, s7
	s_addc_u32 s1, s9, 0
	v_lshlrev_b32_e32 v94, 12, v108
	v_mov_b32_e32 v95, v157
	v_lshl_add_u64 v[0:1], s[0:1], 0, v[94:95]
	v_lshl_add_u64 v[0:1], v[0:1], 0, v[156:157]
	s_mov_b64 s[0:1], 0xc9000
	v_lshl_add_u64 v[158:159], v[0:1], 0, s[0:1]
	s_lshl_b32 s4, s14, 15
	v_lshl_add_u64 v[96:97], v[158:159], 0, s[4:5]
	global_load_dwordx4 v[72:75], v[96:97], off
	global_load_dwordx4 v[8:11], v[96:97], off offset:1024
	global_load_dwordx4 v[4:7], v[96:97], off offset:2048
	global_load_dwordx4 v[0:3], v[96:97], off offset:3072
	v_mul_u32_u24_e32 v95, 0x104, v161
	ds_read_b32 v96, v95 offset:16512
	ds_read_b32 v95, v95 offset:20672
	s_movk_i32 s6, 0x410
	s_movk_i32 s0, 0x104
	v_mov_b32_e32 v97, 0x4080
	s_waitcnt lgkmcnt(1)
	v_lshrrev_b32_e32 v178, 16, v96
	v_and_b32_e32 v96, 0xffff, v96
	v_mad_u32_u24 v176, v161, s0, v97
	v_mad_u32_u24 v110, v109, s6, v96
	s_waitcnt lgkmcnt(0)
	v_lshrrev_b32_e32 v177, 16, v95
	v_and_b32_e32 v95, 0xffff, v95
	s_and_b64 s[0:1], vcc, exec
	v_mad_u32_u24 v111, v109, s6, v95
	s_cselect_b32 s15, 1, -1
	s_or_b32 s0, s7, s4
	ds_read_b128 v[120:123], v110 offset:8192
	ds_read_b128 v[116:119], v111 offset:8192
	v_or3_b32 v92, s0, v94, v156
	v_mov_b32_e32 v93, v157
	v_lshl_add_u64 v[92:93], s[8:9], 0, v[92:93]
	s_mov_b64 s[0:1], 0xc9800
	s_lshl_b32 s4, s15, 1
	v_lshl_add_u64 v[166:167], v[92:93], 0, s[0:1]
	s_ashr_i32 s5, s4, 31
	v_mov_b32_e32 v92, 0
	s_lshl_b64 s[6:7], s[4:5], 15
	s_add_i32 s8, s14, s15
	v_mov_b32_e32 v101, v100
	v_mov_b32_e32 v102, v100
	v_mov_b32_e32 v103, v100
	s_mov_b32 s5, -2
	v_cmp_ne_u32_e64 s[0:1], 1, v92
	v_mov_b32_e32 v96, v157
	v_mov_b32_e32 v97, v157
	v_mov_b32_e32 v98, v157
	v_mov_b32_e32 v99, v157
	v_mov_b32_e32 v92, v157
	v_mov_b32_e32 v93, v157
	v_mov_b32_e32 v94, v157
	v_mov_b32_e32 v95, v157
	v_lshlrev_b32_e32 v162, 4, v108
	v_mul_u32_u24_e32 v157, 0x410, v109
	v_lshlrev_b32_e32 v160, 2, v109
	s_movk_i32 s17, 0x61
	v_add_u32_e32 v226, v162, v160
	v_mul_u32_u24_e32 v226, 12, v226
	v_lshl_add_u32 v229, v161, 4, v157
	v_mul_u32_u24_e32 v230, 0x610, v161
	v_add_u32_e32 v230, v230, v226
	v_add_u32_e32 v231, 0x18400, v226
	s_waitcnt vmcnt(4) lgkmcnt(0)
	ds_read_b128 v[190:193], v229 offset:8192
	ds_read_b128 v[100:103], v229 offset:8448
	ds_read_b128 v[104:107], v229 offset:12864
	ds_read_b128 v[112:115], v229 offset:13120
	s_waitcnt lgkmcnt(3)
	v_mfma_f32_16x16x32_f16 v[194:197], v[60:63], v[190:193], v[84:87]
	v_mfma_f32_16x16x32_f16 v[198:201], v[64:67], v[190:193], v[76:79]
	v_mfma_f32_16x16x32_f16 v[202:205], v[68:71], v[190:193], v[88:91]
	s_waitcnt lgkmcnt(2)
	v_mfma_f32_16x16x32_f16 v[232:235], v[60:63], v[100:103], v[84:87]
	v_mfma_f32_16x16x32_f16 v[236:239], v[64:67], v[100:103], v[76:79]
	v_mfma_f32_16x16x32_f16 v[240:243], v[68:71], v[100:103], v[88:91]
	s_waitcnt lgkmcnt(1)
	v_mfma_f32_16x16x32_f16 v[218:221], v[206:209], v[104:107], v[84:87]
	v_mfma_f32_16x16x32_f16 v[222:225], v[210:213], v[104:107], v[76:79]
	v_mfma_f32_16x16x32_f16 v[244:247], v[214:217], v[104:107], v[88:91]
	s_waitcnt lgkmcnt(0)
	v_mfma_f32_16x16x32_f16 v[182:185], v[206:209], v[112:115], v[84:87]
	v_mfma_f32_16x16x32_f16 v[186:189], v[210:213], v[112:115], v[76:79]
	v_mfma_f32_16x16x32_f16 v[116:119], v[214:217], v[112:115], v[88:91]
	ds_write_b128 v230, v[194:197] offset:24848
	ds_write_b128 v230, v[198:201] offset:24864
	ds_write_b128 v230, v[202:205] offset:24880
	v_add_u32_e32 v230, 0x6100, v230
	ds_write_b128 v230, v[232:235] offset:24848
	ds_write_b128 v230, v[236:239] offset:24864
	ds_write_b128 v230, v[240:243] offset:24880
	v_add_u32_e32 v230, 0x6100, v230
	ds_write_b128 v230, v[218:221] offset:24848
	ds_write_b128 v230, v[222:225] offset:24864
	ds_write_b128 v230, v[244:247] offset:24880
	v_add_u32_e32 v230, 0x6100, v230
	s_nop 7
	s_nop 1
	ds_write_b128 v230, v[182:185] offset:24848
	ds_write_b128 v230, v[186:189] offset:24864
	ds_write_b128 v230, v[116:119] offset:24880
	ds_write_b128 v231, v[84:87] offset:24848
	ds_write_b128 v231, v[76:79] offset:24864
	ds_write_b128 v231, v[88:91] offset:24880
	ds_read_u16 v232, v176
	ds_read_u16 v177, v176 offset:4160
	s_waitcnt lgkmcnt(0)
	v_mad_u32_u24 v227, v232, s17, v226
	ds_read_b128 v[116:119], v227 offset:24848
	ds_read_b128 v[120:123], v227 offset:24864
	ds_read_b128 v[138:141], v227 offset:24880
	v_mov_b32_e32 v182, 0
	v_mov_b32_e32 v183, 0
	v_mov_b32_e32 v184, 0
	v_mov_b32_e32 v185, 0
	v_mov_b32_e32 v222, 0
	v_mov_b32_e32 v223, 0
	v_mov_b32_e32 v224, 0
	v_mov_b32_e32 v225, 0
	v_mov_b32_e32 v186, 0
	v_mov_b32_e32 v187, 0
	v_mov_b32_e32 v188, 0
	v_mov_b32_e32 v189, 0
	v_mov_b32_e32 v100, 0
	v_mov_b32_e32 v101, 0
	v_mov_b32_e32 v102, 0
	v_mov_b32_e32 v103, 0
	v_mov_b32_e32 v104, 0
	v_mov_b32_e32 v105, 0
	v_mov_b32_e32 v106, 0
	v_mov_b32_e32 v107, 0
	v_mov_b32_e32 v108, 0
	v_mov_b32_e32 v109, 0
	v_mov_b32_e32 v110, 0
	v_mov_b32_e32 v111, 0
	v_mov_b32_e32 v112, 0
	v_mov_b32_e32 v113, 0
	v_mov_b32_e32 v114, 0
	v_mov_b32_e32 v115, 0
	v_mov_b32_e32 v206, 0
	v_mov_b32_e32 v207, 0
	v_mov_b32_e32 v208, 0
	v_mov_b32_e32 v209, 0
	v_mov_b32_e32 v210, 0
	v_mov_b32_e32 v211, 0
	v_mov_b32_e32 v212, 0
	v_mov_b32_e32 v213, 0
	v_mov_b32_e32 v214, 0
	v_mov_b32_e32 v215, 0
	v_mov_b32_e32 v216, 0
	v_mov_b32_e32 v217, 0
	v_mov_b32_e32 v218, 0
	v_mov_b32_e32 v219, 0
	v_mov_b32_e32 v220, 0
	v_mov_b32_e32 v221, 0
	s_waitcnt vmcnt(4) lgkmcnt(0)
	v_readfirstlane_b32 s18, v162
	s_nop 3
	s_cmp_ge_u32 s18, 64
	s_cbranch_scc1 .Lgru_loop_b
